# v25 + MoE weight-conversion job pointers (kernarg 0xc0/0xc8/0xd0) and 0x90 cached in free v255 lanes at entry; their per-item serialized s_loads become v_readlane
# speedup vs baseline: 1.0084x; 1.0014x over previous
; #define LAS __attribute__((address_space(3)))
; #define KWS (kargs()->ws)
; __device__ __forceinline__ CJob moe_job(KP P, int j2, int j) {
;     CJob jb; jb.pad = 0; jb.gain = nullptr; jb.mode = 0; jb.fp8 = MOE_FP8 ? 1 : 0; jb.wscale = 1.f; jb.col0 = 0; const int e = j / 3, k = j % 3;
;     if (k < 2) { jb.W = P->in[24 + k] + ((size_t)j2 * NEXP + e) * DM * DFF; jb.gain = P->in[18] + (2 * j2 + 1) * DM; jb.dst = (bf16*)(P->ws + WS_W13E + (size_t)e * 2 * DFF * DM * (MOE_FP8 ? 1 : 2)); jb.K = DM; jb.N = DFF; jb.mode = 4 + k; jb.wscale = MOE_FP8 ? W13_SCALE : 1.f; }
;     else { jb.W = P->in[26] + ((size_t)j2 * NEXP + e) * DFF * DM; jb.dst = (bf16*)(P->ws + WS_W2E + (size_t)e * DM * DFF * (MOE_FP8 ? 1 : 2)); jb.K = DFF; jb.N = DM; jb.wscale = MOE_FP8 ? W2_SCALE : 1.f; }
; __global__ void __launch_bounds__(512, 2) mega(Ptrs Pdummy) {
;     extern __shared__ __attribute__((aligned(16))) unsigned char lds_raw[];
;     LAS unsigned char* lds = (LAS unsigned char*)lds_raw;
;     const int G = (int)gridDim.x, c = (int)blockIdx.x, wbase = __builtin_amdgcn_readfirstlane((int)threadIdx.x) & ~63;
;     { volatile LAS unsigned* MISC0 = (volatile LAS unsigned*)(lds + LDSCTL_OFF); if (threadIdx.x < 64) MISC0[threadIdx.x] = 0u; }
;     __syncthreads();
;     (void)xcd_barrier_post((unsigned*)(KWS + WS_CTL) + CW_BAR, (volatile LAS unsigned*)(lds + LDSCTL_OFF) + 8);
_Z4mega4Ptrs:
	s_mov_b64 s[88:89], s[0:1]
	s_load_dword s60, s[0:1], 0x100
	s_load_dwordx2 s[100:101], s[0:1], 0xf8
	s_load_dwordx4 s[4:7], s[0:1], 0xc0
	s_load_dwordx2 s[8:9], s[0:1], 0xd0
	s_load_dwordx2 s[10:11], s[0:1], 0x90
	s_waitcnt lgkmcnt(0)
	v_writelane_b32 v255, s4, 49
	v_writelane_b32 v255, s5, 50
	v_writelane_b32 v255, s6, 51
	v_writelane_b32 v255, s7, 52
	v_writelane_b32 v255, s8, 53
	v_writelane_b32 v255, s9, 54
	v_writelane_b32 v255, s10, 55
	v_writelane_b32 v255, s11, 56
	s_add_u32 s0, s88, 0x100
	s_addc_u32 s1, s89, 0
	s_mov_b32 s92, s2
	v_writelane_b32 v255, s0, 0
	v_cmp_gt_u32_e32 vcc, 64, v0
	s_nop 0
	v_writelane_b32 v255, s1, 1
	v_readfirstlane_b32 s0, v0
	s_and_saveexec_b64 s[2:3], vcc
	v_lshl_add_u32 v1, v0, 2, 0
	v_add_u32_e32 v1, 0x20000, v1
	v_mov_b32_e32 v2, 0
	ds_write_b32 v1, v2
	s_or_b64 exec, exec, s[2:3]
	s_mov_b64 s[4:5], s[88:89]
	s_waitcnt lgkmcnt(0)
	s_barrier
	s_getreg_b32 s1, hwreg(HW_REG_XCC_ID, 0, 4)
	v_cmp_eq_u32_e32 vcc, 0, v0
	s_and_saveexec_b64 s[2:3], vcc
	s_cbranch_execz .LBB0_5
	s_mov_b64 s[6:7], exec
	v_mbcnt_lo_u32_b32 v0, s6, 0
	v_mbcnt_hi_u32_b32 v0, s7, v0
	v_cmp_eq_u32_e32 vcc, 0, v0
	s_and_b64 s[8:9], exec, vcc
	s_mov_b64 exec, s[8:9]
	s_cbranch_execz .LBB0_5
	s_mov_b64 s[4:5], s[100:101]
	s_lshl_b32 s1, s1, 8
	s_and_b32 s1, s1, 0xf00
	v_mov_b32_e32 v0, 0x4000
	s_waitcnt lgkmcnt(0)
	s_add_u32 s4, s4, s1
	s_addc_u32 s5, s5, 0
	s_bcnt1_i32_b64 s1, s[6:7]
	v_mov_b32_e32 v1, s1
	global_atomic_add v0, v1, s[4:5] offset:1024

; __device__ __forceinline__ CJob static_job(KP P, int j) {
;     ...
;     } else { const int j2 = (j - 24) / 3, k = (j - 24) % 3;
;         const bool f8 = (DENSE_FP8_MASK >> j2) & 1;
;         if (k < 2) { jb.W = P->in[19 + k] + (size_t)j2 * DM * DFF; jb.gain = P->in[18] + (2 * j2) * DM; jb.dst = (bf16*)(P->ws + WS_W13D) + (size_t)j2 * 2 * DFF * DM; jb.K = DM; jb.N = DFF; jb.mode = 4 + k; jb.fp8 = f8; jb.wscale = f8 ? W13_SCALE : 1.f; }
;         else { jb.W = P->in[21] + (size_t)j2 * DFF * DM; jb.dst = (bf16*)(P->ws + WS_W2D) + (size_t)j2 * DM * DFF; jb.K = DFF; jb.N = DM; jb.fp8 = f8; jb.wscale = f8 ? W2_SCALE : 1.f; }
;     }
;     if (jb.ldw == 0) jb.ldw = jb.N;
.LBB0_36:
	s_mov_b32 s15, 0
	s_lshl_b64 s[4:5], s[14:15], 3
	s_add_u32 s4, s10, s4
	s_addc_u32 s5, s11, s5
	s_load_dwordx2 s[4:5], s[4:5], 0x98
	s_and_b64 s[16:17], s[2:3], exec
	v_readlane_b32 s16, v255, 55
	v_readlane_b32 s17, v255, 56
	s_cselect_b32 s1, 0xe00000, 0
	s_waitcnt lgkmcnt(0)
	s_add_u32 s4, s4, s1
	s_addc_u32 s5, s5, 0
	s_and_b64 s[2:3], s[2:3], exec
	s_cselect_b32 s2, 0x2000, 0
	s_add_u32 s2, s16, s2
	s_addc_u32 s3, s17, 0
	s_add_u32 s1, s8, s1
	s_addc_u32 s6, s9, 0
	s_add_u32 s16, s1, 0x4f00000
	s_addc_u32 s17, s6, 0
	s_or_b32 s15, s14, 4
	s_movk_i32 s6, 0xe00
	s_movk_i32 s1, 0x400
	s_mov_b32 s14, 0x42800000

; #define PREF_U(j_) __builtin_amdgcn_readfirstlane(pref[j_])
; __device__ __forceinline__ CJob static_job(KP P, int j) {
;     ...
;     } else { const int j2 = (j - 24) / 3, k = (j - 24) % 3;
;         const bool f8 = (DENSE_FP8_MASK >> j2) & 1;
;         if (k < 2) { jb.W = P->in[19 + k] + (size_t)j2 * DM * DFF; jb.gain = P->in[18] + (2 * j2) * DM; jb.dst = (bf16*)(P->ws + WS_W13D) + (size_t)j2 * 2 * DFF * DM; jb.K = DM; jb.N = DFF; jb.mode = 4 + k; jb.fp8 = f8; jb.wscale = f8 ? W13_SCALE : 1.f; }
;         else { jb.W = P->in[21] + (size_t)j2 * DFF * DM; jb.dst = (bf16*)(P->ws + WS_W2D) + (size_t)j2 * DM * DFF; jb.K = DFF; jb.N = DM; jb.fp8 = f8; jb.wscale = f8 ? W2_SCALE : 1.f; }
;     }
;     if (jb.ldw == 0) jb.ldw = jb.N;
; __device__ __forceinline__ void conv_static_all(KP P, const LAS int* pref, int njobs, LAS float* scr, int gw, int ngw, int lane) {
;     ...
;     for (;;) { const int nx = fl + ngw; const bool has = nx < NT; CJob jn = jb; int jobn = job; f32x4 w[8];
;         if (has) { while (nx >= PREF_U(jobn + 1)) ++jobn; jn = static_job(P, jobn); conv_load(jn, nx - PREF_U(jobn), lane, w); }
.LBB0_76:
	s_andn2_b64 vcc, exec, s[24:25]
	s_mov_b64 s[26:27], 0
	s_cbranch_vccnz .LBB0_121
	s_lshl_b64 s[4:5], s[18:19], 3
	s_add_u32 s4, s10, s4
	s_addc_u32 s5, s11, s5
	s_load_dwordx2 s[4:5], s[4:5], 0x98
	s_and_b64 s[22:23], s[6:7], exec
	v_readlane_b32 s22, v255, 55
	v_readlane_b32 s23, v255, 56
	s_cselect_b32 s28, 0xe00000, 0
	s_waitcnt lgkmcnt(0)
	s_add_u32 s4, s4, s28
	s_addc_u32 s5, s5, 0
	s_and_b64 s[6:7], s[6:7], exec
	s_cselect_b32 s6, 0x2000, 0
	s_add_u32 s24, s22, s6
	s_addc_u32 s25, s23, 0
	s_add_u32 s22, s34, s28
	s_addc_u32 s23, s35, 0
	s_or_b32 s29, s18, 4
	s_movk_i32 s18, 0xe00
	s_movk_i32 s28, 0x400
	s_mov_b32 s6, 0x42800000
	s_branch .LBB0_122

; #define LAS __attribute__((address_space(3)))
; __device__ __forceinline__ CJob moe_job(KP P, int j2, int j) {
;     CJob jb; jb.pad = 0; jb.gain = nullptr; jb.mode = 0; jb.fp8 = MOE_FP8 ? 1 : 0; jb.wscale = 1.f; jb.col0 = 0; const int e = j / 3, k = j % 3;
;     if (k < 2) { jb.W = P->in[24 + k] + ((size_t)j2 * NEXP + e) * DM * DFF; jb.gain = P->in[18] + (2 * j2 + 1) * DM; jb.dst = (bf16*)(P->ws + WS_W13E + (size_t)e * 2 * DFF * DM * (MOE_FP8 ? 1 : 2)); jb.K = DM; jb.N = DFF; jb.mode = 4 + k; jb.wscale = MOE_FP8 ? W13_SCALE : 1.f; }
;     else { jb.W = P->in[26] + ((size_t)j2 * NEXP + e) * DFF * DM; jb.dst = (bf16*)(P->ws + WS_W2E + (size_t)e * DM * DFF * (MOE_FP8 ? 1 : 2)); jb.K = DFF; jb.N = DM; jb.wscale = MOE_FP8 ? W2_SCALE : 1.f; }
;     jb.ldw = jb.N;
;     return jb;
; }
; __device__ __forceinline__ void conv_moe_layer(KP P, int j2, LAS float* scr, int gw, int ngw, int lane) {
;     constexpr int IT = (DM / 64) * (DFF / 32), NT = 24 * IT;
;     int fl = gw; if (fl >= NT) return;
;     CJob jb = moe_job(P, j2, fl / IT); f32x4 v[8]; conv_load(jb, fl % IT, lane, v);
;     for (;;) { const int nx = fl + ngw; const bool has = nx < NT; CJob jn = jb; f32x4 w[8];
;         if (has) { jn = moe_job(P, j2, nx / IT); conv_load(jn, nx % IT, lane, w); }
.LBB0_505:
	s_andn2_b64 vcc, exec, s[62:63]
	s_cbranch_vccnz .LBB0_543
	s_mov_b32 s1, s38
	s_barrier
	s_mov_b64 s[4:5], s[88:89]
	v_mbcnt_lo_u32_b32 v0, s1, 0
	v_mbcnt_hi_u32_b32 v0, s1, v0
	v_add_u32_e32 v0, s93, v0
	s_nop 0
	v_readfirstlane_b32 s1, v0
	s_ashr_i32 s20, s1, 6
	v_readlane_b32 s1, v255, 27
	s_add_i32 s31, s20, s1
	s_cmp_gt_i32 s31, 0xa7ff
	s_cbranch_scc1 .LBB0_542
	s_mul_hi_i32 s1, s31, 0x92492493
	s_add_i32 s1, s1, s31
	s_lshr_b32 s2, s1, 31
	s_ashr_i32 s21, s1, 10
	s_add_i32 s21, s21, s2
	s_mul_hi_i32 s1, s31, 0x30c30c31
	s_lshr_b32 s2, s1, 31
	s_ashr_i32 s13, s1, 10
	s_mul_hi_i32 s1, s21, 0x55555556
	s_add_i32 s13, s13, s2
	s_lshr_b32 s2, s1, 31
	s_add_i32 s1, s1, s2
	s_mul_i32 s1, s1, 3
	s_lshr_b32 s16, s95, 1
	s_sub_i32 s18, s21, s1
	s_cmp_gt_i32 s18, 1
	s_mov_b64 s[2:3], -1
	s_mul_hi_u32 s1, s16, 0x7000000
	s_mul_i32 s12, s16, 0x7000000
	s_cbranch_scc0 .LBB0_509
	s_mov_b32 s17, s40
	s_lshl_b64 s[8:9], s[16:17], 3
	s_ashr_i32 s2, s13, 31
	s_add_u32 s6, s8, s13
	s_addc_u32 s2, s9, s2
	s_mul_i32 s7, s2, 0xe00000
	v_readlane_b32 s2, v255, 53
	v_readlane_b32 s3, v255, 54
	s_mul_hi_u32 s10, s6, 0xe00000
	s_add_i32 s10, s10, s7
	s_mul_i32 s11, s6, 0xe00000
	s_mov_b64 s[6:7], s[100:101]
	s_waitcnt lgkmcnt(0)
	s_add_u32 s14, s2, s11
	s_addc_u32 s15, s3, s10
	s_mul_i32 s3, s13, 0x380000
	s_mul_hi_i32 s2, s13, 0x380000
	s_add_u32 s3, s6, s3
	s_addc_u32 s2, s7, s2
	s_add_u32 s10, s3, 0xea00000
	s_addc_u32 s11, s2, 0
	s_mov_b64 s[2:3], 0
.LBB0_509:
	s_lshl_b32 s6, s16, 11
	s_andn2_b64 vcc, exec, s[2:3]
	s_mov_b32 s7, s40
	s_cbranch_vccnz .LBB0_511
	s_ashr_i32 s19, s18, 31
	s_lshl_b32 s3, s18, 1
	s_add_i32 s3, s3, 49
	v_readlane_b32 s2, v255, s3
	s_add_i32 s3, s3, 1
	v_readlane_b32 s3, v255, s3
	s_mul_i32 s9, s13, 0xe00000
	s_mul_hi_i32 s8, s13, 0xe00000
	s_mul_hi_i32 s10, s13, 0x700000
	s_mul_i32 s13, s13, 0x700000
	s_waitcnt lgkmcnt(0)
	s_add_u32 s2, s2, s9
	s_addc_u32 s3, s3, s8
	s_add_u32 s14, s2, s12
	s_addc_u32 s15, s3, s1
	v_readlane_b32 s2, v255, 55
	v_readlane_b32 s3, v255, 56
	s_lshl_b64 s[8:9], s[6:7], 2
	s_mov_b32 s17, s40
	s_mov_b32 s24, 0x42800000
	s_movk_i32 s33, 0xe00
	s_waitcnt lgkmcnt(0)
	s_add_u32 s2, s2, s8
	s_addc_u32 s3, s3, s9
	s_mov_b64 s[8:9], s[100:101]
	s_add_u32 s2, s2, 0x1000
	s_addc_u32 s3, s3, 0
	s_waitcnt lgkmcnt(0)
	s_add_u32 s8, s8, s13
	s_addc_u32 s9, s9, s10
	s_add_u32 s10, s8, 0x7a00000
	s_addc_u32 s11, s9, 0
	s_add_i32 s30, s18, 4
	s_lshl_b64 s[8:9], s[16:17], 3
	s_movk_i32 s13, 0x400
	s_branch .LBB0_512

; #define LAS __attribute__((address_space(3)))
; __device__ __forceinline__ CJob moe_job(KP P, int j2, int j) {
;     CJob jb; jb.pad = 0; jb.gain = nullptr; jb.mode = 0; jb.fp8 = MOE_FP8 ? 1 : 0; jb.wscale = 1.f; jb.col0 = 0; const int e = j / 3, k = j % 3;
;     if (k < 2) { jb.W = P->in[24 + k] + ((size_t)j2 * NEXP + e) * DM * DFF; jb.gain = P->in[18] + (2 * j2 + 1) * DM; jb.dst = (bf16*)(P->ws + WS_W13E + (size_t)e * 2 * DFF * DM * (MOE_FP8 ? 1 : 2)); jb.K = DM; jb.N = DFF; jb.mode = 4 + k; jb.wscale = MOE_FP8 ? W13_SCALE : 1.f; }
;     else { jb.W = P->in[26] + ((size_t)j2 * NEXP + e) * DFF * DM; jb.dst = (bf16*)(P->ws + WS_W2E + (size_t)e * DM * DFF * (MOE_FP8 ? 1 : 2)); jb.K = DFF; jb.N = DM; jb.wscale = MOE_FP8 ? W2_SCALE : 1.f; }
;     jb.ldw = jb.N;
;     return jb;
; }
; __device__ __forceinline__ void conv_moe_layer(KP P, int j2, LAS float* scr, int gw, int ngw, int lane) {
;     constexpr int IT = (DM / 64) * (DFF / 32), NT = 24 * IT;
;     int fl = gw; if (fl >= NT) return;
;     CJob jb = moe_job(P, j2, fl / IT); f32x4 v[8]; conv_load(jb, fl % IT, lane, v);
;     for (;;) { const int nx = fl + ngw; const bool has = nx < NT; CJob jn = jb; f32x4 w[8];
;         if (has) { jn = moe_job(P, j2, nx / IT); conv_load(jn, nx % IT, lane, w); }
.LBB0_514:
	s_add_i32 s25, s31, s94
	s_cmp_lt_i32 s25, 0xa800
	s_cselect_b64 s[18:19], -1, 0
	s_cmp_gt_i32 s25, 0xa7ff
	s_cbranch_scc1 .LBB0_521
	s_mul_hi_i32 s14, s25, 0x92492493
	s_add_i32 s14, s14, s25
	s_lshr_b32 s15, s14, 31
	s_ashr_i32 s34, s14, 10
	s_add_i32 s34, s34, s15
	s_mul_hi_i32 s14, s25, 0x30c30c31
	s_lshr_b32 s15, s14, 31
	s_ashr_i32 s26, s14, 10
	s_mul_hi_i32 s14, s34, 0x55555556
	s_add_i32 s26, s26, s15
	s_lshr_b32 s15, s14, 31
	s_add_i32 s14, s14, s15
	s_mul_i32 s14, s14, 3
	s_sub_i32 s22, s34, s14
	s_cmp_gt_i32 s22, 1
	s_mov_b64 s[14:15], -1
	s_cbranch_scc0 .LBB0_517
	s_ashr_i32 s14, s26, 31
	s_add_u32 s16, s8, s26
	s_addc_u32 s14, s9, s14
	s_mul_i32 s17, s14, 0xe00000
	v_readlane_b32 s14, v255, 53
	v_readlane_b32 s15, v255, 54
	s_mul_hi_u32 s20, s16, 0xe00000
	s_add_i32 s21, s20, s17
	s_mul_i32 s20, s16, 0xe00000
	s_mov_b64 s[16:17], s[100:101]
	s_waitcnt lgkmcnt(0)
	s_add_u32 s20, s14, s20
	s_addc_u32 s21, s15, s21
	s_mul_i32 s15, s26, 0x380000
	s_mul_hi_i32 s14, s26, 0x380000
	s_add_u32 s15, s16, s15
	s_addc_u32 s14, s17, s14
	s_add_u32 s16, s15, 0xea00000
	s_addc_u32 s17, s14, 0
	s_mov_b64 s[14:15], 0
.LBB0_517:
	s_andn2_b64 vcc, exec, s[14:15]
	s_cbranch_vccnz .LBB0_519
	s_ashr_i32 s23, s22, 31
	s_lshl_b32 s15, s22, 1
	s_add_i32 s15, s15, 49
	v_readlane_b32 s14, v255, s15
	s_add_i32 s15, s15, 1
	v_readlane_b32 s15, v255, s15
	s_mul_i32 s17, s26, 0xe00000
	s_mul_hi_i32 s16, s26, 0xe00000
	s_mul_hi_i32 s23, s26, 0x700000
	s_mul_i32 s26, s26, 0x700000
	s_waitcnt lgkmcnt(0)
	s_add_u32 s14, s14, s17
	s_addc_u32 s15, s15, s16
	s_add_u32 s20, s14, s12
	s_addc_u32 s21, s15, s1
	v_readlane_b32 s14, v255, 55
	v_readlane_b32 s15, v255, 56
	s_lshl_b64 s[16:17], s[6:7], 2
	s_mov_b32 s27, 0x42800000
	s_movk_i32 s28, 0xe00
	s_movk_i32 s29, 0x400
	s_waitcnt lgkmcnt(0)
	s_add_u32 s14, s14, s16
	s_addc_u32 s15, s15, s17
	s_mov_b64 s[16:17], s[100:101]
	s_add_u32 s14, s14, 0x1000
	s_addc_u32 s15, s15, 0
	s_waitcnt lgkmcnt(0)
	s_add_u32 s16, s16, s26
	s_addc_u32 s17, s17, s23
	s_add_u32 s16, s16, 0x7a00000
	s_addc_u32 s17, s17, 0
	s_add_i32 s26, s22, 4
	s_branch .LBB0_520

; #define LAS __attribute__((address_space(3)))
; __device__ __forceinline__ CJob moe_job(KP P, int j2, int j) {
;     CJob jb; jb.pad = 0; jb.gain = nullptr; jb.mode = 0; jb.fp8 = MOE_FP8 ? 1 : 0; jb.wscale = 1.f; jb.col0 = 0; const int e = j / 3, k = j % 3;
;     if (k < 2) { jb.W = P->in[24 + k] + ((size_t)j2 * NEXP + e) * DM * DFF; jb.gain = P->in[18] + (2 * j2 + 1) * DM; jb.dst = (bf16*)(P->ws + WS_W13E + (size_t)e * 2 * DFF * DM * (MOE_FP8 ? 1 : 2)); jb.K = DM; jb.N = DFF; jb.mode = 4 + k; jb.wscale = MOE_FP8 ? W13_SCALE : 1.f; }
;     else { jb.W = P->in[26] + ((size_t)j2 * NEXP + e) * DFF * DM; jb.dst = (bf16*)(P->ws + WS_W2E + (size_t)e * DM * DFF * (MOE_FP8 ? 1 : 2)); jb.K = DFF; jb.N = DM; jb.wscale = MOE_FP8 ? W2_SCALE : 1.f; }
;     jb.ldw = jb.N;
;     return jb;
; }
; __device__ __forceinline__ void conv_moe_layer(KP P, int j2, LAS float* scr, int gw, int ngw, int lane) {
;     constexpr int IT = (DM / 64) * (DFF / 32), NT = 24 * IT;
;     int fl = gw; if (fl >= NT) return;
;     CJob jb = moe_job(P, j2, fl / IT); f32x4 v[8]; conv_load(jb, fl % IT, lane, v);
;     for (;;) { const int nx = fl + ngw; const bool has = nx < NT; CJob jn = jb; f32x4 w[8];
;         if (has) { jn = moe_job(P, j2, nx / IT); conv_load(jn, nx % IT, lane, w); }
.LBB0_642:
	s_or_b64 s[2:3], s[84:85], s[62:63]
	s_and_b64 vcc, exec, s[2:3]
	s_cbranch_vccnz .LBB0_679
	s_mov_b32 s1, s38
	s_barrier
	s_mov_b64 s[4:5], s[88:89]
	v_mbcnt_lo_u32_b32 v0, s1, 0
	v_mbcnt_hi_u32_b32 v0, s1, v0
	v_add_u32_e32 v0, s93, v0
	s_nop 0
	v_readfirstlane_b32 s1, v0
	s_ashr_i32 s18, s1, 6
	v_readlane_b32 s1, v255, 27
	s_add_i32 s31, s18, s1
	s_cmp_gt_i32 s31, 0xa7ff
	s_cbranch_scc1 .LBB0_679
	s_mul_hi_i32 s1, s31, 0x92492493
	s_lshr_b32 s2, s95, 1
	s_mov_b32 s3, s40
	s_add_i32 s1, s1, s31
	s_lshl_b64 s[6:7], s[2:3], 3
	s_lshr_b32 s3, s1, 31
	s_ashr_i32 s19, s1, 10
	s_add_i32 s19, s19, s3
	s_mul_hi_i32 s1, s31, 0x30c30c31
	s_lshr_b32 s3, s1, 31
	s_ashr_i32 s20, s1, 10
	s_mul_hi_i32 s1, s19, 0x55555556
	s_add_i32 s20, s20, s3
	s_lshr_b32 s3, s1, 31
	s_add_i32 s1, s1, s3
	s_mul_i32 s1, s1, 3
	s_sub_i32 s14, s19, s1
	s_cmp_gt_i32 s14, 1
	s_mov_b64 s[16:17], -1
	s_cbranch_scc0 .LBB0_646
	s_ashr_i32 s1, s20, 31
	v_readlane_b32 s8, v255, 53
	v_readlane_b32 s9, v255, 54
	s_mov_b64 s[12:13], s[100:101]
	s_add_u32 s3, s6, s20
	s_addc_u32 s1, s7, s1
	s_mul_i32 s1, s1, 0xe00000
	s_mul_hi_u32 s10, s3, 0xe00000
	s_add_i32 s1, s10, s1
	s_mul_i32 s3, s3, 0xe00000
	s_waitcnt lgkmcnt(0)
	s_add_u32 s10, s8, s3
	s_addc_u32 s11, s9, s1
	s_mul_i32 s3, s20, 0x380000
	s_mul_hi_i32 s1, s20, 0x380000
	s_add_u32 s3, s12, s3
	s_addc_u32 s1, s13, s1
	s_add_u32 s12, s3, 0xea00000
	s_addc_u32 s13, s1, 0
	s_mov_b64 s[16:17], 0
.LBB0_646:
	s_lshl_b32 s8, s2, 11
	s_mov_b32 s9, s40
	s_mul_hi_u32 s1, s2, 0x7000000
	s_andn2_b64 vcc, exec, s[16:17]
	s_mul_i32 s22, s2, 0x7000000
	s_cbranch_vccnz .LBB0_648
	s_ashr_i32 s15, s14, 31
	s_lshl_b32 s3, s14, 1
	s_add_i32 s3, s3, 49
	v_readlane_b32 s2, v255, s3
	s_add_i32 s3, s3, 1
	v_readlane_b32 s3, v255, s3
	s_mul_i32 s11, s20, 0xe00000
	s_mul_hi_i32 s10, s20, 0xe00000
	s_mul_hi_i32 s15, s20, 0x700000
	s_mul_i32 s20, s20, 0x700000
	s_waitcnt lgkmcnt(0)
	s_add_u32 s2, s2, s11
	s_addc_u32 s3, s3, s10
	s_add_u32 s10, s2, s22
	s_addc_u32 s11, s3, s1
	v_readlane_b32 s2, v255, 55
	v_readlane_b32 s3, v255, 56
	s_lshl_b64 s[12:13], s[8:9], 2
	s_mov_b32 s24, 0x42800000
	s_movk_i32 s33, 0xe00
	s_movk_i32 s23, 0x400
	s_waitcnt lgkmcnt(0)
	s_add_u32 s2, s2, s12
	s_addc_u32 s3, s3, s13
	s_mov_b64 s[12:13], s[100:101]
	s_add_u32 s2, s2, 0x1000
	s_addc_u32 s3, s3, 0
	s_waitcnt lgkmcnt(0)
	s_add_u32 s12, s12, s20
	s_addc_u32 s13, s13, s15
	s_add_u32 s12, s12, 0x7a00000
	s_addc_u32 s13, s13, 0
	s_add_i32 s30, s14, 4
	s_branch .LBB0_649

; __device__ __forceinline__ CJob moe_job(KP P, int j2, int j) {
;     CJob jb; jb.pad = 0; jb.gain = nullptr; jb.mode = 0; jb.fp8 = MOE_FP8 ? 1 : 0; jb.wscale = 1.f; jb.col0 = 0; const int e = j / 3, k = j % 3;
;     if (k < 2) { jb.W = P->in[24 + k] + ((size_t)j2 * NEXP + e) * DM * DFF; jb.gain = P->in[18] + (2 * j2 + 1) * DM; jb.dst = (bf16*)(P->ws + WS_W13E + (size_t)e * 2 * DFF * DM * (MOE_FP8 ? 1 : 2)); jb.K = DM; jb.N = DFF; jb.mode = 4 + k; jb.wscale = MOE_FP8 ? W13_SCALE : 1.f; }
;     else { jb.W = P->in[26] + ((size_t)j2 * NEXP + e) * DFF * DM; jb.dst = (bf16*)(P->ws + WS_W2E + (size_t)e * DM * DFF * (MOE_FP8 ? 1 : 2)); jb.K = DFF; jb.N = DM; jb.wscale = MOE_FP8 ? W2_SCALE : 1.f; }
;     jb.ldw = jb.N;
;     return jb;
; }
; __device__ __forceinline__ void conv_moe_layer(KP P, int j2, LAS float* scr, int gw, int ngw, int lane) {
;     ...
;     for (;;) { const int nx = fl + ngw; const bool has = nx < NT; CJob jn = jb; f32x4 w[8];
;         if (has) { jn = moe_job(P, j2, nx / IT); conv_load(jn, nx % IT, lane, w); }
.LBB0_651:
	s_add_i32 s25, s31, s94
	s_cmp_lt_i32 s25, 0xa800
	s_cselect_b64 s[18:19], -1, 0
	s_cmp_gt_i32 s25, 0xa7ff
	s_cbranch_scc1 .LBB0_658
	s_mul_hi_i32 s10, s25, 0x92492493
	s_add_i32 s10, s10, s25
	s_lshr_b32 s11, s10, 31
	s_ashr_i32 s34, s10, 10
	s_add_i32 s34, s34, s11
	s_mul_hi_i32 s10, s25, 0x30c30c31
	s_lshr_b32 s11, s10, 31
	s_ashr_i32 s26, s10, 10
	s_mul_hi_i32 s10, s34, 0x55555556
	s_add_i32 s26, s26, s11
	s_lshr_b32 s11, s10, 31
	s_add_i32 s10, s10, s11
	s_mul_i32 s10, s10, 3
	s_sub_i32 s20, s34, s10
	s_cmp_gt_i32 s20, 1
	s_mov_b64 s[14:15], -1
	s_cbranch_scc0 .LBB0_654
	s_ashr_i32 s10, s26, 31
	s_add_u32 s14, s6, s26
	s_addc_u32 s10, s7, s10
	s_mul_i32 s15, s10, 0xe00000
	v_readlane_b32 s10, v255, 53
	v_readlane_b32 s11, v255, 54
	s_mul_hi_u32 s16, s14, 0xe00000
	s_add_i32 s16, s16, s15
	s_mul_i32 s17, s14, 0xe00000
	s_mov_b64 s[14:15], s[100:101]
	s_waitcnt lgkmcnt(0)
	s_add_u32 s10, s10, s17
	s_addc_u32 s11, s11, s16
	s_mul_i32 s17, s26, 0x380000
	s_mul_hi_i32 s16, s26, 0x380000
	s_add_u32 s14, s14, s17
	s_addc_u32 s15, s15, s16
	s_add_u32 s16, s14, 0xea00000
	s_addc_u32 s17, s15, 0
	s_mov_b64 s[14:15], 0
.LBB0_654:
	s_andn2_b64 vcc, exec, s[14:15]
	s_cbranch_vccnz .LBB0_656
	s_ashr_i32 s21, s20, 31
	s_lshl_b32 s11, s20, 1
	s_add_i32 s11, s11, 49
	v_readlane_b32 s10, v255, s11
	s_add_i32 s11, s11, 1
	v_readlane_b32 s11, v255, s11
	s_mul_i32 s15, s26, 0xe00000
	s_mul_hi_i32 s14, s26, 0xe00000
	s_mul_hi_i32 s21, s26, 0x700000
	s_mul_i32 s26, s26, 0x700000
	s_waitcnt lgkmcnt(0)
	s_add_u32 s10, s10, s15
	s_addc_u32 s11, s11, s14
	v_readlane_b32 s14, v255, 55
	v_readlane_b32 s15, v255, 56
	s_add_u32 s10, s10, s22
	s_addc_u32 s11, s11, s1
	s_lshl_b64 s[16:17], s[8:9], 2
	s_mov_b32 s27, 0x42800000
	s_waitcnt lgkmcnt(0)
	s_add_u32 s14, s14, s16
	s_addc_u32 s15, s15, s17
	s_mov_b64 s[16:17], s[100:101]
	s_add_u32 s14, s14, 0x1000
	s_addc_u32 s15, s15, 0
	s_movk_i32 s28, 0xe00
	s_movk_i32 s29, 0x400
	s_waitcnt lgkmcnt(0)
	s_add_u32 s16, s16, s26
	s_addc_u32 s17, s17, s21
	s_add_u32 s16, s16, 0x7a00000
	s_addc_u32 s17, s17, 0
	s_add_i32 s26, s20, 4
	s_branch .LBB0_657

; #define LAS __attribute__((address_space(3)))
; __device__ __forceinline__ int opaque_tid(int wbase) { int t = wbase + lane_id(); asm volatile("" : "+v"(t)); return t; }
; __device__ __forceinline__ int opaque_s(int x) { asm volatile("" : "+s"(x)); return x; }
; __device__ __forceinline__ void route_a(LAS unsigned char* lds, const bf16* h, const float* ssq, const float* gain, const float* rw, const float* rb, int* sel, float* selw, int* CNT, int G, int c, int wbase) {
;     const int tid = opaque_tid(wbase), lane = tid & 63, wid = __builtin_amdgcn_readfirstlane(tid >> 6); LAS int* lc = (LAS int*)lds; G = opaque_s(G); c = opaque_s(c);
;     f32x4 wg[4][4][2];
; #pragma unroll
;     for (int j = 0; j < 4; ++j) { const f32x4 gk = *(const f32x4*)(gain + 4 * lane + 256 * j);
; #pragma unroll
;         for (int q = 0; q < 4; ++q) { const float* wp = rw + (size_t)(4 * lane + 256 * j + q) * 8; wg[j][q][0] = *(const f32x4*)wp * gk[q]; wg[j][q][1] = *(const f32x4*)(wp + 4) * gk[q]; } }
;     float rbv[8];
; #pragma unroll
;     for (int e = 0; e < 8; ++e) rbv[e] = rb[e];
.LBB0_1104:
	s_or_b64 exec, exec, s[36:37]
	v_readlane_b32 s2, v255, 31
	v_readlane_b32 s3, v255, 32
	s_andn2_b64 vcc, exec, s[2:3]
	s_mov_b64 s[2:3], -1
	s_waitcnt lgkmcnt(0)
	s_barrier
	s_cbranch_vccnz .LBB0_1616
	s_mov_b64 s[8:9], s[88:89]
	s_mov_b64 s[4:5], s[88:89]
	s_mov_b64 s[6:7], s[88:89]
	s_mov_b64 s[2:3], s[88:89]
	s_mov_b32 s1, s38
	v_readlane_b32 s10, v255, 4
	v_mbcnt_lo_u32_b32 v0, s1, 0
	v_mbcnt_hi_u32_b32 v0, s1, v0
	v_add_u32_e32 v170, s93, v0
	s_mov_b32 s1, s10
	s_mov_b32 s33, s92
	s_cmpk_lt_i32 s33, 0x100
	v_readfirstlane_b32 s12, v170
	v_readlane_b32 s11, v255, 5
	s_cbranch_scc0 .LBB0_1118
	s_mov_b64 s[24:25], s[100:101]
	s_nop 0
	v_readlane_b32 s4, v255, 55
	v_readlane_b32 s5, v255, 56
	v_readlane_b32 s8, v255, 33
	s_lshr_b32 s13, s95, 1
	v_readlane_b32 s9, v255, 34
	s_load_dwordx2 s[6:7], s[6:7], 0xb0
	s_lshl_b32 s10, s13, 13
	s_lshl_b32 s14, s13, 3
	s_lshl_b64 s[8:9], s[8:9], 2
	s_waitcnt lgkmcnt(0)
	s_add_u32 s4, s4, s8
	v_and_b32_e32 v8, 63, v170
	s_mov_b32 s11, s40
	s_addc_u32 s5, s5, s9
	v_lshlrev_b32_e32 v2, 4, v8
	s_lshl_b64 s[8:9], s[10:11], 2
	global_load_dwordx4 v[4:7], v2, s[4:5]
	s_add_u32 s6, s6, s8
	s_addc_u32 s7, s7, s9
	v_lshlrev_b32_e32 v232, 7, v8
	s_load_dwordx2 s[2:3], s[2:3], 0xb8
	global_load_dwordx4 v[10:13], v232, s[6:7] offset:48
	global_load_dwordx4 v[24:27], v232, s[6:7] offset:32
	global_load_dwordx4 v[20:23], v232, s[6:7] offset:16
	global_load_dwordx4 v[16:19], v232, s[6:7]
	v_lshl_add_u64 v[0:1], s[6:7], 0, v[232:233]
	v_lshl_add_u64 v[14:15], v[0:1], 0, s[70:71]
	s_mov_b32 s15, s40
	s_lshl_b64 s[8:9], s[14:15], 2
	s_waitcnt lgkmcnt(0)
	s_add_u32 s2, s2, s8
	s_addc_u32 s3, s3, s9
	s_add_u32 s34, s24, 0x17600000
	s_addc_u32 s35, s25, 0
	s_add_u32 s36, s24, 0x17640000
	s_addc_u32 s37, s25, 0
	s_add_u32 s10, s24, 0x177f1000
	s_addc_u32 s11, s25, 0
	v_and_b32_e32 v9, 3, v170
	s_mov_b32 s41, 0
	v_lshl_add_u32 v171, v170, 2, 0
	s_waitcnt vmcnt(3)
	v_pk_mul_f32 v[28:29], v[4:5], v[10:11] op_sel:[1,0]
	v_pk_mul_f32 v[30:31], v[4:5], v[12:13] op_sel:[1,0]
	global_load_dwordx4 v[10:13], v232, s[6:7] offset:112
	global_load_dwordx4 v[40:43], v232, s[6:7] offset:96
	global_load_dwordx4 v[36:39], v232, s[6:7] offset:80
	global_load_dwordx4 v[32:35], v232, s[6:7] offset:64
	s_movk_i32 s6, 0x2000
	v_add_co_u32_e32 v64, vcc, s6, v0
	s_waitcnt vmcnt(4)
	v_pk_mul_f32 v[16:17], v[4:5], v[16:17] op_sel_hi:[0,1]
	v_pk_mul_f32 v[18:19], v[4:5], v[18:19] op_sel_hi:[0,1]
	v_pk_mul_f32 v[20:21], v[4:5], v[20:21] op_sel_hi:[0,1]
	v_pk_mul_f32 v[22:23], v[4:5], v[22:23] op_sel_hi:[0,1]
	v_pk_mul_f32 v[24:25], v[4:5], v[24:25] op_sel:[1,0]
	v_pk_mul_f32 v[26:27], v[4:5], v[26:27] op_sel:[1,0]
	v_mov_b32_e32 v4, v7
	v_addc_co_u32_e32 v65, vcc, 0, v1, vcc
	s_mov_b64 s[6:7], 0x2040
	s_waitcnt vmcnt(3)
	v_pk_mul_f32 v[44:45], v[4:5], v[10:11] op_sel_hi:[0,1]
	s_waitcnt vmcnt(2)
	v_pk_mul_f32 v[40:41], v[4:5], v[40:41] op_sel_hi:[0,1]
	s_waitcnt vmcnt(1)
	v_pk_mul_f32 v[36:37], v[6:7], v[36:37] op_sel_hi:[0,1]
	s_waitcnt vmcnt(0)
	v_pk_mul_f32 v[32:33], v[6:7], v[32:33] op_sel_hi:[0,1]
	v_pk_mul_f32 v[34:35], v[6:7], v[34:35] op_sel_hi:[0,1]
	v_pk_mul_f32 v[38:39], v[6:7], v[38:39] op_sel_hi:[0,1]
	v_pk_mul_f32 v[42:43], v[4:5], v[42:43] op_sel_hi:[0,1]
	v_pk_mul_f32 v[46:47], v[4:5], v[12:13] op_sel_hi:[0,1]
	global_load_dwordx4 v[4:7], v2, s[4:5] offset:1024
	global_load_dwordx4 v[10:13], v[64:65], off
	global_load_dwordx4 v[60:63], v[14:15], off offset:48
	global_load_dwordx4 v[56:59], v[14:15], off offset:32
	global_load_dwordx4 v[52:55], v[14:15], off offset:16
	s_waitcnt vmcnt(3)
	v_pk_mul_f32 v[48:49], v[4:5], v[12:13] op_sel_hi:[0,1]
	v_pk_mul_f32 v[50:51], v[4:5], v[10:11] op_sel_hi:[0,1]
	s_waitcnt vmcnt(0)
	v_pk_mul_f32 v[52:53], v[4:5], v[52:53] op_sel_hi:[0,1]
	v_pk_mul_f32 v[54:55], v[4:5], v[54:55] op_sel_hi:[0,1]
	v_pk_mul_f32 v[56:57], v[4:5], v[56:57] op_sel:[1,0]
	v_pk_mul_f32 v[58:59], v[4:5], v[58:59] op_sel:[1,0]
	v_pk_mul_f32 v[60:61], v[4:5], v[60:61] op_sel:[1,0]
	v_pk_mul_f32 v[62:63], v[4:5], v[62:63] op_sel:[1,0]
	v_lshl_add_u64 v[4:5], v[0:1], 0, s[6:7]
	global_load_dwordx4 v[10:13], v[64:65], off offset:64
	global_load_dwordx4 v[76:79], v[4:5], off offset:48
	global_load_dwordx4 v[72:75], v[4:5], off offset:32
	global_load_dwordx4 v[68:71], v[4:5], off offset:16
	s_mov_b64 s[6:7], 0x4000
	v_lshl_add_u64 v[14:15], v[0:1], 0, s[6:7]
	s_movk_i32 s6, 0x4000
	v_add_co_u32_e32 v96, vcc, s6, v0
	v_mov_b32_e32 v4, v7
	s_nop 0
	v_addc_co_u32_e32 v97, vcc, 0, v1, vcc
	s_mov_b64 s[6:7], 0x4040
	s_waitcnt vmcnt(3)
; __device__ __forceinline__ void route_a(LAS unsigned char* lds, const bf16* h, const float* ssq, const float* gain, const float* rw, const float* rb, int* sel, float* selw, int* CNT, int G, int c, int wbase) {
;     ...
;     for (int j = 0; j < 4; ++j) { const f32x4 gk = *(const f32x4*)(gain + 4 * lane + 256 * j);
; #pragma unroll
;         for (int q = 0; q < 4; ++q) { const float* wp = rw + (size_t)(4 * lane + 256 * j + q) * 8; wg[j][q][0] = *(const f32x4*)wp * gk[q]; wg[j][q][1] = *(const f32x4*)(wp + 4) * gk[q]; } }
;     float rbv[8];
; #pragma unroll
;     for (int e = 0; e < 8; ++e) rbv[e] = rb[e];
;     for (int chunk = c; chunk < NCHUNK; chunk += G) {
	v_pk_mul_f32 v[64:65], v[6:7], v[12:13] op_sel_hi:[0,1]
	v_pk_mul_f32 v[66:67], v[6:7], v[10:11] op_sel_hi:[0,1]
	s_waitcnt vmcnt(1)
	v_pk_mul_f32 v[72:73], v[4:5], v[72:73] op_sel_hi:[0,1]
	s_waitcnt vmcnt(0)
	v_pk_mul_f32 v[68:69], v[6:7], v[68:69] op_sel_hi:[0,1]
	v_pk_mul_f32 v[70:71], v[6:7], v[70:71] op_sel_hi:[0,1]
	v_pk_mul_f32 v[74:75], v[4:5], v[74:75] op_sel_hi:[0,1]
	v_pk_mul_f32 v[76:77], v[4:5], v[76:77] op_sel_hi:[0,1]
	v_pk_mul_f32 v[78:79], v[4:5], v[78:79] op_sel_hi:[0,1]
	global_load_dwordx4 v[4:7], v2, s[4:5] offset:2048
	global_load_dwordx4 v[10:13], v[96:97], off
	global_load_dwordx4 v[92:95], v[14:15], off offset:48
	global_load_dwordx4 v[88:91], v[14:15], off offset:32
	global_load_dwordx4 v[84:87], v[14:15], off offset:16
	s_waitcnt vmcnt(3)
	v_pk_mul_f32 v[80:81], v[4:5], v[12:13] op_sel_hi:[0,1]
	v_pk_mul_f32 v[82:83], v[4:5], v[10:11] op_sel_hi:[0,1]
	s_waitcnt vmcnt(0)
	v_pk_mul_f32 v[84:85], v[4:5], v[84:85] op_sel_hi:[0,1]
	v_pk_mul_f32 v[86:87], v[4:5], v[86:87] op_sel_hi:[0,1]
	v_pk_mul_f32 v[88:89], v[4:5], v[88:89] op_sel:[1,0]
	v_pk_mul_f32 v[90:91], v[4:5], v[90:91] op_sel:[1,0]
	v_pk_mul_f32 v[92:93], v[4:5], v[92:93] op_sel:[1,0]
	v_pk_mul_f32 v[94:95], v[4:5], v[94:95] op_sel:[1,0]
	v_lshl_add_u64 v[4:5], v[0:1], 0, s[6:7]
	global_load_dwordx4 v[10:13], v[96:97], off offset:64
	global_load_dwordx4 v[108:111], v[4:5], off offset:48
	global_load_dwordx4 v[104:107], v[4:5], off offset:32
	global_load_dwordx4 v[100:103], v[4:5], off offset:16
	v_mov_b32_e32 v4, v7
	s_waitcnt vmcnt(3)
	v_pk_mul_f32 v[96:97], v[6:7], v[12:13] op_sel_hi:[0,1]
	s_waitcnt vmcnt(2)
	v_pk_mul_f32 v[108:109], v[4:5], v[108:109] op_sel_hi:[0,1]
	s_waitcnt vmcnt(1)
	v_pk_mul_f32 v[104:105], v[4:5], v[104:105] op_sel_hi:[0,1]
	v_pk_mul_f32 v[106:107], v[4:5], v[106:107] op_sel_hi:[0,1]
	v_pk_mul_f32 v[110:111], v[4:5], v[110:111] op_sel_hi:[0,1]
	global_load_dwordx4 v[2:5], v2, s[4:5] offset:3072
	s_mov_b64 s[4:5], 0x6000
	v_pk_mul_f32 v[98:99], v[6:7], v[10:11] op_sel_hi:[0,1]
	s_waitcnt vmcnt(1)
	v_pk_mul_f32 v[100:101], v[6:7], v[100:101] op_sel_hi:[0,1]
	v_pk_mul_f32 v[102:103], v[6:7], v[102:103] op_sel_hi:[0,1]
	v_lshl_add_u64 v[6:7], v[0:1], 0, s[4:5]
	s_movk_i32 s4, 0x6000
	v_add_co_u32_e32 v14, vcc, s4, v0
	s_mov_b64 s[4:5], 0x6040
	s_nop 0
	v_addc_co_u32_e32 v15, vcc, 0, v1, vcc
	global_load_dwordx4 v[10:13], v[14:15], off
	global_load_dwordx4 v[124:127], v[6:7], off offset:48
	global_load_dwordx4 v[120:123], v[6:7], off offset:32
	global_load_dwordx4 v[116:119], v[6:7], off offset:16
	v_lshl_add_u64 v[6:7], v[0:1], 0, s[4:5]
	v_cmp_eq_u32_e64 s[4:5], 0, v8
	s_waitcnt vmcnt(3)
	v_pk_mul_f32 v[112:113], v[2:3], v[12:13] op_sel_hi:[0,1]
	v_pk_mul_f32 v[114:115], v[2:3], v[10:11] op_sel_hi:[0,1]
	s_waitcnt vmcnt(1)
	v_pk_mul_f32 v[120:121], v[2:3], v[120:121] op_sel:[1,0]
	s_waitcnt vmcnt(0)
	v_pk_mul_f32 v[116:117], v[2:3], v[116:117] op_sel_hi:[0,1]
	v_pk_mul_f32 v[118:119], v[2:3], v[118:119] op_sel_hi:[0,1]
	v_pk_mul_f32 v[122:123], v[2:3], v[122:123] op_sel:[1,0]
	v_pk_mul_f32 v[124:125], v[2:3], v[124:125] op_sel:[1,0]
	v_pk_mul_f32 v[126:127], v[2:3], v[126:127] op_sel:[1,0]
	global_load_dwordx4 v[0:3], v[14:15], off offset:64
	global_load_dwordx4 v[10:13], v[6:7], off offset:48
	global_load_dwordx4 v[136:139], v[6:7], off offset:32
	global_load_dwordx4 v[132:135], v[6:7], off offset:16
	s_waitcnt vmcnt(3)
	v_pk_mul_f32 v[130:131], v[4:5], v[0:1] op_sel_hi:[0,1]
	v_mov_b32_e32 v0, v5
	v_pk_mul_f32 v[128:129], v[4:5], v[2:3] op_sel_hi:[0,1]
	s_waitcnt vmcnt(0)
	v_pk_mul_f32 v[132:133], v[4:5], v[132:133] op_sel_hi:[0,1]
	v_pk_mul_f32 v[134:135], v[4:5], v[134:135] op_sel_hi:[0,1]
	v_pk_mul_f32 v[136:137], v[0:1], v[136:137] op_sel_hi:[0,1]
	v_pk_mul_f32 v[138:139], v[0:1], v[138:139] op_sel_hi:[0,1]
	v_pk_mul_f32 v[140:141], v[0:1], v[10:11] op_sel_hi:[0,1]
	v_pk_mul_f32 v[142:143], v[0:1], v[12:13] op_sel_hi:[0,1]
	global_load_dwordx4 v[0:3], v233, s[2:3]
	global_load_dwordx4 v[4:7], v233, s[2:3] offset:16
	v_readlane_b32 s2, v255, 10
	s_cmp_eq_u32 s2, 0
	s_mov_b32 s2, 0x13200000
	s_cselect_b32 s6, s2, 0x1b800000
	s_ashr_i32 s2, s12, 2
	s_and_b32 s7, s2, -16
	s_lshl_b32 s2, s2, 1
	s_lshl_b32 s42, s33, 8
	s_andn2_b32 s2, s2, 31
	s_add_i32 s42, s42, s2
	s_lshl_b32 s43, s1, 8
	v_readlane_b32 s2, v255, 11
	s_cmp_eq_u32 s2, 1
	s_cselect_b32 s8, 0, 0x200000
	v_lshl_or_b32 v232, v9, 4, s8
	s_mov_b64 s[8:9], 0x17200000
	v_lshl_add_u64 v[144:145], v[232:233], 0, s[8:9]
	s_lshl_b32 s8, s33, 7
	s_add_i32 s26, s8, s7
	v_cmp_gt_i32_e64 s[2:3], 8, v170
	s_or_b32 s28, s26, 1
	s_lshl_b32 s44, s1, 7
	v_lshl_or_b32 v232, v8, 3, s6
	s_branch .LBB0_1108
